# baseline (speedup 1.0000x reference)
.Lk_220:
	s_lshr_b32 s0, s14, 6
	s_mul_i32 s1, s0, 0x1c2
	s_add_u32 s1, s1, s33
	v_and_b32_e32 v1, 63, v0
	v_and_b32_e32 v2, 1, v0
	v_add_u32_e32 v2, 64, v2
	v_add_u32_e32 v3, s1, v1
	v_add_u32_e32 v4, s1, v2
	v_lshlrev_b32_e32 v5, 4, v3
	v_lshlrev_b32_e32 v3, 2, v3
	v_lshlrev_b32_e32 v6, 4, v4
	v_lshlrev_b32_e32 v4, 2, v4
	global_load_dwordx4 v[84:87], v5, s[54:55]
	global_load_dword v92, v3, s[56:57]
	global_load_dwordx4 v[88:91], v6, s[54:55]
	global_load_dword v93, v4, s[56:57]
	s_lshl_b32 s0, s0, 2
	v_lshlrev_b32_e32 v94, 6, v1
	v_add_u32_e32 v94, s0, v94
	v_lshlrev_b32_e32 v95, 2, v94
	v_add_u32_e32 v94, 0x1c200, v94
	v_lshlrev_b32_e32 v96, 6, v2
	v_add_u32_e32 v96, s0, v96
	v_lshlrev_b32_e32 v97, 2, v96
	v_add_u32_e32 v96, 0x1c200, v96
	s_mov_b64 s[0:1], exec

.Lk_232:
	s_waitcnt vmcnt(13)
	v_fma_mixlo_f16 v52, v46, v58, 0
	v_fma_mixlo_f16 v53, v46, v58, -v52 op_sel_hi:[0,0,1]
	v_cvt_f16_f32_e32 v58, v57
	v_cmp_eq_u32_e32 vcc, 1, v54
	v_cmp_gt_u32_e64 s[0:1], 16, v80
	v_cvt_f16_f32_e32 v64, v51
	v_cvt_f32_f16_e32 v60, v58
	v_cndmask_b32_e32 v53, 0, v53, vcc
	v_cndmask_b32_e64 v65, v53, v52, s[0:1]
	v_cvt_f32_f16_e32 v61, v64
	v_sub_f32_e32 v53, v57, v60
	v_cvt_f16_f32_e32 v53, v53
	v_cvt_f16_f32_e32 v57, v59
	v_cndmask_b32_e64 v67, 0, v52, s[0:1]
	v_sub_f32_e32 v51, v51, v61
	v_cndmask_b32_e32 v53, 0, v53, vcc
	v_cndmask_b32_e64 v66, v53, v58, s[0:1]
	v_cvt_f32_f16_e32 v53, v57
	v_cndmask_b32_e64 v68, 0, v58, s[0:1]
	s_waitcnt vmcnt(2)
	v_pk_mul_f32 v[16:17], v[46:47], v[16:17] op_sel_hi:[0,1]
	v_pk_mul_f32 v[18:19], v[46:47], v[18:19] op_sel_hi:[0,1]
	v_sub_f32_e32 v52, v59, v53
	v_cvt_f16_f32_e32 v69, v52
	global_load_dword v52, v[2:3], off offset:4
	global_load_dword v53, v[2:3], off offset:260
	global_load_dword v58, v[2:3], off offset:516
	global_load_dword v59, v[2:3], off offset:772
	global_load_dword v60, v[4:5], off offset:4
	global_load_dword v61, v[4:5], off offset:260
	global_load_dword v62, v[4:5], off offset:516
	global_load_dword v63, v[4:5], off offset:772
	v_pk_mul_f32 v[20:21], v[46:47], v[20:21] op_sel_hi:[0,1]
	v_pk_mul_f32 v[22:23], v[46:47], v[22:23] op_sel_hi:[0,1]
	v_pk_mul_f32 v[24:25], v[46:47], v[24:25] op_sel_hi:[0,1]
	v_pk_mul_f32 v[26:27], v[46:47], v[26:27] op_sel_hi:[0,1]
	v_cvt_pk_f16_f32 v16, v16, v17
	v_cvt_pk_f16_f32 v17, v18, v19
	v_pk_mul_f32 v[18:19], v[46:47], v[32:33] op_sel_hi:[0,1]
	v_pk_mul_f32 v[32:33], v[46:47], v[34:35] op_sel_hi:[0,1]
	v_cvt_pk_f16_f32 v20, v20, v21
	v_cvt_pk_f16_f32 v21, v22, v23
	v_pk_mul_f32 v[22:23], v[46:47], v[28:29] op_sel_hi:[0,1]
	v_pk_mul_f32 v[28:29], v[46:47], v[30:31] op_sel_hi:[0,1]
	v_cvt_pk_f16_f32 v24, v24, v25
	v_cvt_pk_f16_f32 v25, v26, v27
	v_cvt_f16_f32_e32 v26, v50
	v_cvt_pk_f16_f32 v18, v18, v19
	v_cvt_pk_f16_f32 v19, v32, v33
	v_cvt_pk_f16_f32 v22, v22, v23
	v_cvt_pk_f16_f32 v23, v28, v29
	v_cvt_f16_f32_e32 v29, v56
	v_cvt_f16_f32_e32 v32, v55
	v_cvt_f32_f16_e32 v30, v26
	v_cvt_f16_f32_e32 v51, v51
	v_cvt_f32_f16_e32 v31, v29
	v_cvt_f32_f16_e32 v33, v32
	v_sub_f32_e32 v30, v50, v30
	v_cvt_f16_f32_e32 v30, v30
	v_sub_f32_e32 v31, v56, v31
	v_sub_f32_e32 v33, v55, v33
	v_cvt_f16_f32_e32 v31, v31
	v_cvt_f16_f32_e32 v33, v33
	v_pk_mul_f32 v[12:13], v[46:47], v[12:13] op_sel_hi:[0,1]
	v_pk_mul_f32 v[14:15], v[46:47], v[14:15] op_sel_hi:[0,1]
	s_waitcnt vmcnt(8)
	v_fma_mixlo_f16 v27, v46, v45, 0
	v_cvt_pk_f16_f32 v12, v12, v13
	v_cvt_pk_f16_f32 v13, v14, v15
	v_pk_mul_f32 v[14:15], v[46:47], v[36:37] op_sel_hi:[0,1]
	v_pk_mul_f32 v[36:37], v[46:47], v[38:39] op_sel_hi:[0,1]
	v_fma_mixlo_f16 v28, v46, v45, -v27 op_sel_hi:[0,0,1]
	v_cndmask_b32_e32 v30, 0, v30, vcc
	v_cvt_pk_f16_f32 v14, v14, v15
	v_cvt_pk_f16_f32 v15, v36, v37
	v_cndmask_b32_e32 v28, 0, v28, vcc
	v_cndmask_b32_e64 v30, v30, v26, s[0:1]
	v_cndmask_b32_e32 v31, 0, v31, vcc
	v_cndmask_b32_e64 v36, 0, v26, s[0:1]
	v_cndmask_b32_e32 v26, 0, v33, vcc
	v_cndmask_b32_e32 v51, 0, v51, vcc
	v_cndmask_b32_e32 v2, 0, v69, vcc
	s_mov_b32 s8, 0x4038aa3b
	v_and_b32_e32 v34, 15, v0
	v_cndmask_b32_e64 v28, v28, v27, s[0:1]
	v_cndmask_b32_e64 v31, v31, v29, s[0:1]
	v_cndmask_b32_e64 v35, 0, v27, s[0:1]
	v_cndmask_b32_e64 v26, v26, v32, s[0:1]
	v_cndmask_b32_e64 v51, v51, v64, s[0:1]
	v_cndmask_b32_e64 v4, 0, v64, s[0:1]
	v_cndmask_b32_e64 v5, 0, v57, s[0:1]
	v_cndmask_b32_e64 v2, v2, v57, s[0:1]
	s_mov_b32 s9, 0xbfb8aa3b
	v_cndmask_b32_e64 v29, 0, v29, s[0:1]
	v_cndmask_b32_e64 v33, 0, v32, s[0:1]
	v_pack_b32_f16 v27, v31, v26
	v_pack_b32_f16 v26, v28, v30
	v_pack_b32_f16 v28, v35, v36
	s_lshl_b32 s0, s15, 8
	v_lshlrev_b32_e32 v81, 4, v34
	v_lshlrev_b32_e32 v35, 2, v54
	s_mov_b32 s7, 0
	v_pk_add_f32 v[6:7], v[6:7], v[8:9]
	v_pk_add_f32 v[8:9], v[10:11], v[48:49]
	s_mov_b32 s6, s9
	v_pk_mul_f32 v[10:11], v[46:47], v[40:41] op_sel_hi:[0,1]
	v_pk_mul_f32 v[40:41], v[46:47], v[42:43] op_sel_hi:[0,1]
	v_pack_b32_f16 v29, v29, v33
	v_lshlrev_b32_e32 v74, 4, v80
	v_or3_b32 v35, v81, v35, s0
	s_waitcnt vmcnt(2)
	v_pk_add_f32 v[30:31], v[52:53], v[60:61]
	v_pack_b32_f16 v3, v51, v2
	s_waitcnt vmcnt(0)
	v_pk_add_f32 v[32:33], v[58:59], v[62:63]
	v_pack_b32_f16 v2, v65, v66
	v_pack_b32_f16 v5, v4, v5
	v_pack_b32_f16 v4, v67, v68
	v_pk_mul_f32 v[8:9], v[8:9], s[8:9]
	v_pk_mul_f32 v[6:7], v[6:7], s[6:7] op_sel_hi:[1,0]
	v_cvt_pk_f16_f32 v10, v10, v11
	v_cvt_pk_f16_f32 v11, v40, v41
	v_pk_mul_f32 v[32:33], v[32:33], s[8:9]
	v_pk_mul_f32 v[30:31], v[30:31], s[6:7] op_sel_hi:[1,0]
	v_add_u32_e32 v78, 0x23280, v74
	v_add_u32_e32 v79, 0x23280, v35
	s_mov_b64 s[0:1], -1
	s_and_b64 vcc, exec, s[4:5]
	s_waitcnt vmcnt(0)
	v_cvt_pk_f16_f32 v108, v84, v85
	v_cvt_pk_f16_f32 v109, v86, v87
	v_cvt_f16_f32_e32 v116, v92
	v_cvt_f32_f16_e32 v112, v108
	v_cvt_f32_f16_sdwa v113, v108 dst_sel:DWORD dst_unused:UNUSED_PAD src0_sel:WORD_1
	v_cvt_f32_f16_e32 v114, v109
	v_cvt_f32_f16_sdwa v115, v109 dst_sel:DWORD dst_unused:UNUSED_PAD src0_sel:WORD_1
	v_cvt_f32_f16_e32 v116, v116
	v_pk_add_f32 v[112:113], v[84:85], v[112:113] neg_lo:[0,1] neg_hi:[0,1]
	v_pk_add_f32 v[114:115], v[86:87], v[114:115] neg_lo:[0,1] neg_hi:[0,1]
	v_sub_f32_e32 v116, v92, v116
	v_cvt_pk_f16_f32 v110, v112, v113
	v_cvt_pk_f16_f32 v111, v114, v115
	v_cvt_pk_f16_f32 v116, v92, v116
	ds_write_b128 v95, v[108:111]
	ds_write_b32 v94, v116
	v_cvt_pk_f16_f32 v108, v88, v89
	v_cvt_pk_f16_f32 v109, v90, v91
	v_cvt_f16_f32_e32 v116, v93
	v_cvt_f32_f16_e32 v112, v108
	v_cvt_f32_f16_sdwa v113, v108 dst_sel:DWORD dst_unused:UNUSED_PAD src0_sel:WORD_1
	v_cvt_f32_f16_e32 v114, v109
	v_cvt_f32_f16_sdwa v115, v109 dst_sel:DWORD dst_unused:UNUSED_PAD src0_sel:WORD_1
	v_cvt_f32_f16_e32 v116, v116
	v_pk_add_f32 v[112:113], v[88:89], v[112:113] neg_lo:[0,1] neg_hi:[0,1]
	v_pk_add_f32 v[114:115], v[90:91], v[114:115] neg_lo:[0,1] neg_hi:[0,1]
	v_sub_f32_e32 v116, v93, v116
	v_cvt_pk_f16_f32 v110, v112, v113
	v_cvt_pk_f16_f32 v111, v114, v115
	v_cvt_pk_f16_f32 v116, v93, v116
	ds_write_b128 v97, v[108:111]
	ds_write_b32 v96, v116
	s_waitcnt lgkmcnt(0)
	s_barrier
	s_cbranch_vccz .Lk_298
	s_setprio 0
	v_and_b32_e32 v34, 15, v80
	v_lshrrev_b32_e32 v35, 4, v80
	s_and_b32 s10, s15, 1
	v_lshrrev_b32_e32 v36, 2, v34
	v_and_b32_e32 v37, 3, v34
	v_lshl_add_u32 v36, v36, 3, v37
	s_lshl_b32 s11, s10, 2
	v_add_u32_e32 v36, s11, v36
	v_lshlrev_b32_e32 v36, 9, v36
	v_lshl_add_u32 v36, v35, 5, v36
	global_load_dwordx4 v[44:47], v36, s[42:43] offset:0
	global_load_dwordx4 v[48:51], v36, s[42:43] offset:16
	global_load_dwordx4 v[52:55], v36, s[42:43] offset:128
	global_load_dwordx4 v[56:59], v36, s[42:43] offset:144
	global_load_dwordx4 v[60:63], v36, s[42:43] offset:256
	global_load_dwordx4 v[64:67], v36, s[42:43] offset:272
	global_load_dwordx4 v[68:71], v36, s[42:43] offset:384
	global_load_dwordx4 v[72:75], v36, s[42:43] offset:400
	v_lshlrev_b32_e32 v37, 5, v35
	s_lshl_b32 s12, s10, 4
	v_add_u32_e32 v37, s12, v37
	global_load_dwordx4 v[120:123], v37, s[44:45]
	s_mul_i32 s12, s3, 0x70800
	s_add_u32 s16, s22, s12
	s_addc_u32 s17, s23, 0
	s_lshl_b32 s12, s3, 8
	s_add_u32 s18, s24, s12
	s_addc_u32 s19, s25, 0
	s_add_u32 s18, s18, s11
	s_addc_u32 s19, s19, 0
	v_lshlrev_b32_e32 v38, 4, v80
	s_lshl_b32 s12, s10, 3
	v_add_u32_e32 v38, s12, v38
	v_lshlrev_b32_e32 v39, 2, v34
	v_add_u32_e32 v39, 0x1c200, v39
	s_mov_b32 s0, 0x4038aa3b
	s_mov_b32 s1, 0
	s_mov_b32 s9, 2
	s_waitcnt vmcnt(0)
	v_cvt_pk_f16_f32 v104, v44, v45
	v_cvt_pk_f16_f32 v105, v46, v47
	v_cvt_pk_f16_f32 v106, v48, v49
	v_cvt_pk_f16_f32 v107, v50, v51
	v_cvt_pk_f16_f32 v108, v52, v53
	v_cvt_pk_f16_f32 v109, v54, v55
	v_cvt_pk_f16_f32 v110, v56, v57
	v_cvt_pk_f16_f32 v111, v58, v59
	v_cvt_pk_f16_f32 v112, v60, v61
	v_cvt_pk_f16_f32 v113, v62, v63
	v_cvt_pk_f16_f32 v114, v64, v65
	v_cvt_pk_f16_f32 v115, v66, v67
	v_cvt_pk_f16_f32 v116, v68, v69
	v_cvt_pk_f16_f32 v117, v70, v71
	v_cvt_pk_f16_f32 v118, v72, v73
	v_cvt_pk_f16_f32 v119, v74, v75
	ds_read_b32 v64, v39
	v_mov_b32_e32 v40, 0
	v_mov_b32_e32 v41, 0
	v_mov_b32_e32 v61, 0
	v_mov_b32_e32 v63, 0
	v_mov_b32_e32 v83, 0
	v_mov_b32_e32 v58, 0xc038aa3b
	v_mov_b32_e32 v59, 0xc038aa3b
	s_waitcnt lgkmcnt(0)
	v_and_b32_e32 v60, 0xffff, v64
	v_lshrrev_b32_e32 v62, 16, v64
	s_nop 1
	v_mfma_f32_16x16x32_f16 v[50:53], v[2:5], v[60:63], v[6:9]
	v_mfma_f32_16x16x32_f16 v[54:57], v[26:29], v[60:63], v[30:33]
	ds_read_b128 v[42:45], v78 offset:6144
	ds_read_b128 v[46:49], v78 offset:7168
	s_waitcnt lgkmcnt(1)
	v_mfma_f32_16x16x32_f16 v[50:53], v[18:21], v[42:45], v[50:53]
	v_mfma_f32_16x16x32_f16 v[54:57], v[10:13], v[42:45], v[54:57]
	s_waitcnt lgkmcnt(0)
	v_mfma_f32_16x16x32_f16 v[50:53], v[22:25], v[46:49], v[50:53]
	v_mfma_f32_16x16x32_f16 v[54:57], v[14:17], v[46:49], v[54:57]
	ds_read_b32 v64, v39 offset:64
	s_nop 7
	v_exp_f32_e32 v84, v52
	v_exp_f32_e32 v85, v56
	v_exp_f32_e32 v86, v50
	v_exp_f32_e32 v87, v54
	v_exp_f32_e32 v88, v51
	v_exp_f32_e32 v89, v55
	v_pk_add_f32 v[90:91], v[84:85], 1.0 op_sel_hi:[1,0]
	v_pk_fma_f32 v[92:93], v[84:85], s[0:1], v[58:59] op_sel_hi:[1,0,0]
	v_pk_fma_f32 v[90:91], v[86:87], v[90:91], v[90:91]
	v_pk_fma_f32 v[94:95], v[90:91], v[88:89], v[90:91]
	v_rcp_f32_e32 v94, v94
	v_rcp_f32_e32 v95, v95
	v_pk_fma_f32 v[92:93], v[92:93], v[88:89], v[92:93]
	v_pk_fma_f32 v[92:93], v[40:41], v[90:91], v[92:93]
	v_exp_f32_e32 v96, v53
	v_pk_mul_f32 v[40:41], v[92:93], v[94:95]
	v_exp_f32_e32 v98, v40
	v_exp_f32_e32 v99, v41
	v_exp_f32_e32 v97, v57
	v_pk_add_f32 v[100:101], v[98:99], 1.0 op_sel_hi:[1,0]
	v_pk_fma_f32 v[100:101], v[100:101], v[96:97], v[100:101]
	v_rcp_f32_e32 v100, v100
	v_rcp_f32_e32 v101, v101
	v_pk_add_f32 v[102:103], v[98:99], -1.0 op_sel_hi:[1,0]
	v_pk_mul_f32 v[102:103], v[102:103], v[100:101]
	v_cvt_pk_f16_f32 v126, v102, v103
	ds_write_b32 v79, v126 offset:4096
	s_waitcnt lgkmcnt(1)
	v_and_b32_e32 v60, 0xffff, v64
	v_lshrrev_b32_e32 v62, 16, v64
	s_nop 1
	v_mfma_f32_16x16x32_f16 v[50:53], v[2:5], v[60:63], v[6:9]
	v_mfma_f32_16x16x32_f16 v[54:57], v[26:29], v[60:63], v[30:33]
	s_waitcnt lgkmcnt(0)
	s_barrier
	s_cmp_lt_u32 s15, 2
	s_cbranch_scc0 .Lpb_nc_1
	ds_read_b128 v[66:69], v78 offset:0
	ds_read_b128 v[70:73], v78 offset:1024
